# speedup vs baseline: 1.0319x; 1.0093x over previous
.LBB1_3:
	s_mov_b32 s29, s16
	v_add_u32_e32 v0, s29, v101
	ds_read_b128 v[94:97], v0 offset:16384
	ds_read_b128 v[102:105], v0 offset:17408
	ds_read_b128 v[106:109], v0 offset:18432
	ds_read_b128 v[110:113], v0 offset:19456
	ds_read_b128 v[114:117], v0 offset:32768
	ds_read_b128 v[118:121], v0 offset:33792
	ds_read_b128 v[122:125], v0 offset:34816
	ds_read_b128 v[126:129], v0 offset:35840
	v_add_u32_e32 v0, s29, v91
	ds_read_b128 v[130:133], v0
	ds_read_b128 v[134:137], v0 offset:1024
	ds_read_b128 v[138:141], v0 offset:2048
	ds_read_b128 v[142:145], v0 offset:3072
	ds_read_b128 v[146:149], v0 offset:4096
	ds_read_b128 v[150:153], v0 offset:5120
	ds_read_b128 v[154:157], v0 offset:6144
	ds_read_b128 v[158:161], v0 offset:7168
	s_lshl_b32 s16, s28, 2
	s_or_b32 s16, s16, s23
	s_lshl_b64 s[30:31], s[16:17], 19
	s_add_u32 s16, s6, s30
	s_addc_u32 s31, s7, s31
	s_lshl_b32 s33, s3, 7
	s_ashr_i32 s35, s33, 31
	s_add_u32 s30, s16, s33
	s_addc_u32 s31, s31, s35
	s_add_u32 s34, s4, s33
	s_addc_u32 s35, s5, s35
	s_add_i32 s16, s19, s27
	s_add_i32 m0, s16, 0x4000
	s_nop 0
	global_load_lds_dwordx4 v84, s[30:31]
	s_add_i32 m0, s16, 0x6000
	s_nop 0
	global_load_lds_dwordx4 v88, s[30:31]
	s_mov_b32 m0, s16
	s_nop 0
	global_load_lds_dwordx4 v82, s[34:35]
	s_waitcnt vmcnt(3)
	s_waitcnt lgkmcnt(0)
	s_barrier
	s_setprio 1
	s_waitcnt lgkmcnt(0)
	v_mfma_f32_16x16x32_f16 v[78:81], v[94:97], v[130:133], v[78:81]
	v_mfma_f32_16x16x32_f16 v[74:77], v[106:109], v[130:133], v[74:77]
	v_mfma_f32_16x16x32_f16 v[66:69], v[94:97], v[138:141], v[66:69]
	v_mfma_f32_16x16x32_f16 v[58:61], v[106:109], v[138:141], v[58:61]
	v_mfma_f32_16x16x32_f16 v[78:81], v[102:105], v[134:137], v[78:81]
	s_add_u32 s30, s30, 0x40000
	v_mfma_f32_16x16x32_f16 v[74:77], v[110:113], v[134:137], v[74:77]
	s_addc_u32 s31, s31, 0
	s_add_i32 m0, s16, 0x8000
	v_mfma_f32_16x16x32_f16 v[66:69], v[102:105], v[142:145], v[66:69]
	v_mfma_f32_16x16x32_f16 v[58:61], v[110:113], v[142:145], v[58:61]
	global_load_lds_dwordx4 v84, s[30:31]
	v_mfma_f32_16x16x32_f16 v[54:57], v[94:97], v[146:149], v[54:57]
	v_mfma_f32_16x16x32_f16 v[46:49], v[106:109], v[146:149], v[46:49]
	v_mfma_f32_16x16x32_f16 v[34:37], v[94:97], v[154:157], v[34:37]
	v_mfma_f32_16x16x32_f16 v[26:29], v[106:109], v[154:157], v[26:29]
	v_mfma_f32_16x16x32_f16 v[54:57], v[102:105], v[150:153], v[54:57]
	v_mfma_f32_16x16x32_f16 v[46:49], v[110:113], v[150:153], v[46:49]
	s_add_i32 m0, s16, 0xa000
	v_mfma_f32_16x16x32_f16 v[34:37], v[102:105], v[158:161], v[34:37]
	v_mfma_f32_16x16x32_f16 v[26:29], v[110:113], v[158:161], v[26:29]
	global_load_lds_dwordx4 v88, s[30:31]
	v_mfma_f32_16x16x32_f16 v[70:73], v[114:117], v[130:133], v[70:73]
	v_mfma_f32_16x16x32_f16 v[62:65], v[122:125], v[130:133], v[62:65]
	v_mfma_f32_16x16x32_f16 v[50:53], v[114:117], v[138:141], v[50:53]
	v_mfma_f32_16x16x32_f16 v[42:45], v[122:125], v[138:141], v[42:45]
	v_mfma_f32_16x16x32_f16 v[70:73], v[118:121], v[134:137], v[70:73]
	v_mfma_f32_16x16x32_f16 v[62:65], v[126:129], v[134:137], v[62:65]
	s_add_i32 m0, s16, 0x2000
	v_mfma_f32_16x16x32_f16 v[50:53], v[118:121], v[142:145], v[50:53]
	v_mfma_f32_16x16x32_f16 v[42:45], v[126:129], v[142:145], v[42:45]
	global_load_lds_dwordx4 v86, s[34:35]
	v_mfma_f32_16x16x32_f16 v[38:41], v[114:117], v[146:149], v[38:41]
	v_mfma_f32_16x16x32_f16 v[30:33], v[122:125], v[146:149], v[30:33]
	v_mfma_f32_16x16x32_f16 v[22:25], v[114:117], v[154:157], v[22:25]
	v_mfma_f32_16x16x32_f16 v[2:5], v[122:125], v[154:157], v[2:5]
	v_mfma_f32_16x16x32_f16 v[38:41], v[118:121], v[150:153], v[38:41]
	v_mfma_f32_16x16x32_f16 v[30:33], v[126:129], v[150:153], v[30:33]
	v_mfma_f32_16x16x32_f16 v[22:25], v[118:121], v[158:161], v[22:25]
	v_mfma_f32_16x16x32_f16 v[2:5], v[126:129], v[158:161], v[2:5]
	s_setprio 0
	s_add_i32 s3, s3, 1
	s_cmp_lt_u32 s28, 2
	s_cselect_b64 s[30:31], -1, 0
	s_cmp_eq_u32 s3, 16
	s_cselect_b64 s[34:35], -1, 0
	s_and_b64 s[36:37], s[34:35], exec
	s_cselect_b32 s3, 0, s3
	s_and_b64 s[30:31], s[34:35], s[30:31]
	s_cmp_lg_u64 s[30:31], 0
	s_addc_u32 s28, s28, 0
	s_barrier
	s_add_i32 s26, s26, -1
	s_mov_b32 s16, s24
	s_mov_b32 s24, s27
	s_cmp_lg_u32 s26, 0
	s_mov_b32 s27, s29
	s_cbranch_scc1 .LBB1_3
	s_lshl_b32 s3, s14, 7
	s_add_i32 s17, s25, s3
	s_ashr_i32 s3, s17, 1
	s_lshr_b32 s14, s17, 5
	s_or_b32 s24, s15, s2
	s_and_b32 s14, s14, 62
	s_and_b32 s27, s3, 0xfffffc00
	v_or_b32_e32 v105, s24, v1
	v_lshlrev_b32_e32 v98, 4, v93
	v_or_b32_e32 v102, 16, v93
	v_or_b32_e32 v103, 32, v93
	v_or_b32_e32 v104, 48, v93
	v_mov_b32_e32 v93, 0
	s_and_b32 s16, s24, 0x340
	v_lshlrev_b32_e32 v95, 6, v105
	s_or_b32 s2, s27, s14
	v_lshlrev_b32_e32 v0, 9, v92
	v_and_b32_e32 v110, 0xc00, v95
	v_mov_b32_e32 v111, v93
	s_or_b32 s14, s2, s16
	v_and_b32_e32 v92, 0x200, v0
	v_lshl_add_u64 v[110:111], s[8:9], 0, v[110:111]
	s_or_b32 s30, s14, 0x80
	s_mov_b32 s3, 0
	v_mov_b32_e32 v99, v93
	v_lshl_add_u64 v[110:111], v[110:111], 0, v[92:93]
	s_mov_b32 s2, 0x3e38aa3b
	v_pk_add_f32 v[72:73], v[12:13], v[72:73]
	v_pk_add_f32 v[70:71], v[10:11], v[70:71]
	v_pk_add_f32 v[64:65], v[8:9], v[64:65]
	v_pk_add_f32 v[62:63], v[6:7], v[62:63]
	s_ashr_i32 s31, s30, 31
	v_lshl_add_u64 v[112:113], v[110:111], 0, v[98:99]
	v_pk_mul_f32 v[72:73], v[72:73], s[2:3] op_sel_hi:[1,0]
	v_pk_mul_f32 v[70:71], v[70:71], s[2:3] op_sel_hi:[1,0]
	v_pk_mul_f32 v[64:65], v[64:65], s[2:3] op_sel_hi:[1,0]
	v_pk_mul_f32 v[62:63], v[62:63], s[2:3] op_sel_hi:[1,0]
	s_lshl_b64 s[30:31], s[30:31], 12
	v_lshlrev_b32_e32 v96, 4, v102
	v_mov_b32_e32 v97, v93
	v_pk_add_f32 v[80:81], v[20:21], v[80:81]
	v_pk_add_f32 v[78:79], v[18:19], v[78:79]
	v_pk_add_f32 v[74:75], v[14:15], v[74:75]
	s_ashr_i32 s15, s14, 31
	v_cvt_pk_f16_f32 v70, v70, v71
	v_cvt_pk_f16_f32 v71, v72, v73
	v_cvt_pk_f16_f32 v72, v62, v63
	v_cvt_pk_f16_f32 v73, v64, v65
	v_lshl_add_u64 v[62:63], v[112:113], 0, s[30:31]
	v_pk_add_f32 v[58:59], v[14:15], v[58:59]
	v_pk_mul_f32 v[80:81], v[80:81], s[2:3] op_sel_hi:[1,0]
	v_pk_mul_f32 v[78:79], v[78:79], s[2:3] op_sel_hi:[1,0]
	v_pk_mul_f32 v[74:75], v[74:75], s[2:3] op_sel_hi:[1,0]
	s_lshl_b64 s[28:29], s[14:15], 12
	global_store_dwordx4 v[62:63], v[70:73], off sc1
	v_pk_add_f32 v[62:63], v[20:21], v[68:69]
	v_pk_add_f32 v[64:65], v[18:19], v[66:67]
	v_lshl_add_u64 v[70:71], v[110:111], 0, v[96:97]
	v_pk_mul_f32 v[58:59], v[58:59], s[2:3] op_sel_hi:[1,0]
	v_pk_add_f32 v[52:53], v[12:13], v[52:53]
	v_pk_add_f32 v[50:51], v[10:11], v[50:51]
	v_pk_add_f32 v[44:45], v[8:9], v[44:45]
	v_pk_add_f32 v[42:43], v[6:7], v[42:43]
	v_lshlrev_b32_e32 v0, 4, v103
	v_cvt_pk_f16_f32 v78, v78, v79
	v_cvt_pk_f16_f32 v79, v80, v81
	v_cvt_pk_f16_f32 v80, v74, v75
	v_lshl_add_u64 v[74:75], v[112:113], 0, s[28:29]
	v_pk_mul_f32 v[66:67], v[62:63], s[2:3] op_sel_hi:[1,0]
	v_pk_mul_f32 v[62:63], v[64:65], s[2:3] op_sel_hi:[1,0]
	v_cvt_pk_f16_f32 v64, v58, v59
	v_lshl_add_u64 v[58:59], v[70:71], 0, s[28:29]
	v_pk_mul_f32 v[52:53], v[52:53], s[2:3] op_sel_hi:[1,0]
	v_pk_mul_f32 v[50:51], v[50:51], s[2:3] op_sel_hi:[1,0]
	v_pk_mul_f32 v[44:45], v[44:45], s[2:3] op_sel_hi:[1,0]
	v_pk_mul_f32 v[42:43], v[42:43], s[2:3] op_sel_hi:[1,0]
	s_or_b32 s28, s14, 1
	s_or_b32 s14, s14, 0x81
	v_and_b32_e32 v106, 0xf0, v0
	v_mov_b32_e32 v107, v93
	v_cvt_pk_f16_f32 v50, v50, v51
	v_cvt_pk_f16_f32 v51, v52, v53
	v_cvt_pk_f16_f32 v52, v42, v43
	v_cvt_pk_f16_f32 v53, v44, v45
	v_lshl_add_u64 v[42:43], v[70:71], 0, s[30:31]
	v_pk_add_f32 v[40:41], v[12:13], v[40:41]
	v_pk_add_f32 v[38:39], v[10:11], v[38:39]
	v_pk_add_f32 v[32:33], v[8:9], v[32:33]
	v_pk_add_f32 v[30:31], v[6:7], v[30:31]
	s_ashr_i32 s15, s14, 31
	v_lshlrev_b32_e32 v94, 4, v104
	global_store_dwordx4 v[42:43], v[50:53], off sc1
	v_pk_mul_f32 v[40:41], v[40:41], s[2:3] op_sel_hi:[1,0]
	v_pk_mul_f32 v[38:39], v[38:39], s[2:3] op_sel_hi:[1,0]
	v_lshl_add_u64 v[50:51], v[110:111], 0, v[106:107]
	v_pk_mul_f32 v[32:33], v[32:33], s[2:3] op_sel_hi:[1,0]
	v_pk_mul_f32 v[30:31], v[30:31], s[2:3] op_sel_hi:[1,0]
	s_lshl_b64 s[14:15], s[14:15], 12
	v_and_b32_e32 v108, 0x1f0, v94
	v_mov_b32_e32 v109, v93
	v_pk_add_f32 v[42:43], v[20:21], v[56:57]
	v_pk_add_f32 v[44:45], v[18:19], v[54:55]
	v_pk_add_f32 v[46:47], v[14:15], v[46:47]
	s_ashr_i32 s29, s28, 31
	v_cvt_pk_f16_f32 v38, v38, v39
	v_cvt_pk_f16_f32 v39, v40, v41
	v_cvt_pk_f16_f32 v40, v30, v31
	v_cvt_pk_f16_f32 v41, v32, v33
	v_lshl_add_u64 v[30:31], v[50:51], 0, s[14:15]
	v_pk_add_f32 v[20:21], v[20:21], v[36:37]
	v_pk_add_f32 v[18:19], v[18:19], v[34:35]
	v_pk_add_f32 v[14:15], v[14:15], v[26:27]
	v_pk_add_f32 v[76:77], v[16:17], v[76:77]
	v_pk_add_f32 v[60:61], v[16:17], v[60:61]
	v_pk_mul_f32 v[52:53], v[42:43], s[2:3] op_sel_hi:[1,0]
	v_pk_mul_f32 v[42:43], v[44:45], s[2:3] op_sel_hi:[1,0]
	v_pk_add_f32 v[44:45], v[16:17], v[48:49]
	s_lshl_b64 s[28:29], s[28:29], 12
	global_store_dwordx4 v[30:31], v[38:41], off sc1
	v_lshl_add_u64 v[30:31], v[110:111], 0, v[108:109]
	v_pk_mul_f32 v[20:21], v[20:21], s[2:3] op_sel_hi:[1,0]
	v_pk_mul_f32 v[18:19], v[18:19], s[2:3] op_sel_hi:[1,0]
	v_pk_add_f32 v[16:17], v[16:17], v[28:29]
	v_pk_mul_f32 v[14:15], v[14:15], s[2:3] op_sel_hi:[1,0]
	v_pk_add_f32 v[12:13], v[12:13], v[24:25]
	v_pk_add_f32 v[10:11], v[10:11], v[22:23]
	v_pk_add_f32 v[4:5], v[8:9], v[4:5]
	v_pk_add_f32 v[2:3], v[6:7], v[2:3]
	v_pk_mul_f32 v[76:77], v[76:77], s[2:3] op_sel_hi:[1,0]
	v_pk_mul_f32 v[60:61], v[60:61], s[2:3] op_sel_hi:[1,0]
	v_pk_mul_f32 v[48:49], v[44:45], s[2:3] op_sel_hi:[1,0]
	v_pk_mul_f32 v[44:45], v[46:47], s[2:3] op_sel_hi:[1,0]
	v_lshl_add_u64 v[46:47], v[50:51], 0, s[28:29]
	v_cvt_pk_f16_f32 v18, v18, v19
	v_cvt_pk_f16_f32 v19, v20, v21
	v_pk_mul_f32 v[16:17], v[16:17], s[2:3] op_sel_hi:[1,0]
	v_cvt_pk_f16_f32 v20, v14, v15
	v_lshl_add_u64 v[14:15], v[30:31], 0, s[28:29]
	v_pk_mul_f32 v[12:13], v[12:13], s[2:3] op_sel_hi:[1,0]
	v_pk_mul_f32 v[10:11], v[10:11], s[2:3] op_sel_hi:[1,0]
	v_pk_mul_f32 v[4:5], v[4:5], s[2:3] op_sel_hi:[1,0]
	v_pk_mul_f32 v[2:3], v[2:3], s[2:3] op_sel_hi:[1,0]
	s_add_u32 s28, s20, s22
	v_cvt_pk_f16_f32 v81, v76, v77
	v_cvt_pk_f16_f32 v62, v62, v63
	v_cvt_pk_f16_f32 v63, v66, v67
	v_cvt_pk_f16_f32 v65, v60, v61
	v_cvt_pk_f16_f32 v42, v42, v43
	v_cvt_pk_f16_f32 v43, v52, v53
	v_cvt_pk_f16_f32 v44, v44, v45
	v_cvt_pk_f16_f32 v45, v48, v49
	v_cvt_pk_f16_f32 v21, v16, v17
	v_cvt_pk_f16_f32 v10, v10, v11
	v_cvt_pk_f16_f32 v11, v12, v13
	v_cvt_pk_f16_f32 v12, v2, v3
	v_cvt_pk_f16_f32 v13, v4, v5
	v_lshl_add_u64 v[2:3], v[30:31], 0, s[14:15]
	s_addc_u32 s29, s21, 0
	v_lshlrev_b32_e32 v92, 2, v1
	global_store_dwordx4 v[74:75], v[78:81], off sc1
	global_store_dwordx4 v[58:59], v[62:65], off sc1
	global_store_dwordx4 v[46:47], v[42:45], off sc1
	global_store_dwordx4 v[14:15], v[18:21], off sc1
	global_store_dwordx4 v[2:3], v[10:13], off sc1
	v_lshl_add_u64 v[2:3], s[28:29], 0, v[92:93]
	s_mov_b64 s[28:29], 0x1000
	v_lshl_add_u64 v[10:11], v[2:3], 0, s[28:29]
	global_load_dwordx4 v[22:25], v[10:11], off
	global_load_dwordx4 v[14:17], v[10:11], off offset:16
	global_load_dwordx4 v[6:9], v[10:11], off offset:512
	global_load_dwordx4 v[2:5], v[10:11], off offset:528
	s_mov_b32 s25, 1
	s_mov_b32 s26, 16
	s_mov_b32 s14, 2
	s_mov_b32 s15, 0x18000
	s_mov_b32 s2, 0xc000
	s_mov_b32 s27, 0
	v_mov_b32_e32 v10, v93
	v_mov_b32_e32 v11, v93
	v_mov_b32_e32 v12, v93
	v_mov_b32_e32 v13, v93
	v_mov_b32_e32 v18, v93
	v_mov_b32_e32 v19, v93
	v_mov_b32_e32 v20, v93
	v_mov_b32_e32 v21, v93
	v_mov_b32_e32 v26, v93
	v_mov_b32_e32 v27, v93
	v_mov_b32_e32 v28, v93
	v_mov_b32_e32 v29, v93
	v_mov_b32_e32 v34, v93
	v_mov_b32_e32 v35, v93
	v_mov_b32_e32 v36, v93
	v_mov_b32_e32 v37, v93
	v_mov_b32_e32 v42, v93
	v_mov_b32_e32 v43, v93
	v_mov_b32_e32 v44, v93
	v_mov_b32_e32 v45, v93
	v_mov_b32_e32 v50, v93
	v_mov_b32_e32 v51, v93
	v_mov_b32_e32 v52, v93
	v_mov_b32_e32 v53, v93
	v_mov_b32_e32 v62, v93
	v_mov_b32_e32 v63, v93
	v_mov_b32_e32 v64, v93
	v_mov_b32_e32 v65, v93
	v_mov_b32_e32 v70, v93
	v_mov_b32_e32 v71, v93
	v_mov_b32_e32 v72, v93
	v_mov_b32_e32 v73, v93
	v_mov_b32_e32 v30, v93
	v_mov_b32_e32 v31, v93
	v_mov_b32_e32 v32, v93
	v_mov_b32_e32 v33, v93
	v_mov_b32_e32 v38, v93
	v_mov_b32_e32 v39, v93
	v_mov_b32_e32 v40, v93
	v_mov_b32_e32 v41, v93
	v_mov_b32_e32 v46, v93
	v_mov_b32_e32 v47, v93
	v_mov_b32_e32 v48, v93
	v_mov_b32_e32 v49, v93
	v_mov_b32_e32 v54, v93
	v_mov_b32_e32 v55, v93
	v_mov_b32_e32 v56, v93
	v_mov_b32_e32 v57, v93
	v_mov_b32_e32 v58, v93
	v_mov_b32_e32 v59, v93
	v_mov_b32_e32 v60, v93
	v_mov_b32_e32 v61, v93
	v_mov_b32_e32 v66, v93
	v_mov_b32_e32 v67, v93
	v_mov_b32_e32 v68, v93
	v_mov_b32_e32 v69, v93
	v_mov_b32_e32 v74, v93
	v_mov_b32_e32 v75, v93
	v_mov_b32_e32 v76, v93
	v_mov_b32_e32 v77, v93
	v_mov_b32_e32 v78, v93
	v_mov_b32_e32 v79, v93
	v_mov_b32_e32 v80, v93
	v_mov_b32_e32 v81, v93
.LBB1_5:
	s_mov_b32 s28, s2
	v_add_u32_e32 v1, s28, v101
	ds_read_b128 v[106:109], v1 offset:16384
	ds_read_b128 v[110:113], v1 offset:17408
	ds_read_b128 v[114:117], v1 offset:18432
	ds_read_b128 v[118:121], v1 offset:19456
	ds_read_b128 v[122:125], v1 offset:32768
	ds_read_b128 v[126:129], v1 offset:33792
	ds_read_b128 v[130:133], v1 offset:34816
	ds_read_b128 v[134:137], v1 offset:35840
	v_add_u32_e32 v1, s28, v91
	ds_read_b128 v[138:141], v1
	ds_read_b128 v[142:145], v1 offset:1024
	ds_read_b128 v[146:149], v1 offset:2048
	ds_read_b128 v[150:153], v1 offset:3072
	ds_read_b128 v[154:157], v1 offset:4096
	ds_read_b128 v[158:161], v1 offset:5120
	ds_read_b128 v[162:165], v1 offset:6144
	ds_read_b128 v[166:169], v1 offset:7168
	s_lshl_b32 s2, s25, 2
	s_or_b32 s2, s2, s23
	s_lshl_b64 s[30:31], s[2:3], 19
	s_add_u32 s2, s6, s30
	s_addc_u32 s29, s7, s31
	s_lshl_b32 s33, s14, 7
	s_ashr_i32 s35, s33, 31
	s_add_u32 s30, s2, s33
	s_addc_u32 s31, s29, s35
	s_add_u32 s34, s4, s33
	s_addc_u32 s35, s5, s35
	s_add_i32 s2, s19, s27
	s_add_i32 m0, s2, 0x4000
	s_nop 0
	global_load_lds_dwordx4 v84, s[30:31]
	s_add_i32 m0, s2, 0x6000
	s_nop 0
	global_load_lds_dwordx4 v88, s[30:31]
	s_mov_b32 m0, s2
	s_nop 0
	global_load_lds_dwordx4 v82, s[34:35]
	s_waitcnt vmcnt(3)
	s_waitcnt lgkmcnt(0)
	s_barrier
	s_setprio 1
	s_waitcnt lgkmcnt(0)
	v_mfma_f32_16x16x32_f16 v[78:81], v[106:109], v[138:141], v[78:81]
	v_mfma_f32_16x16x32_f16 v[74:77], v[114:117], v[138:141], v[74:77]
	v_mfma_f32_16x16x32_f16 v[66:69], v[106:109], v[146:149], v[66:69]
	v_mfma_f32_16x16x32_f16 v[58:61], v[114:117], v[146:149], v[58:61]
	v_mfma_f32_16x16x32_f16 v[78:81], v[110:113], v[142:145], v[78:81]
	s_add_u32 s30, s30, 0x40000
	v_mfma_f32_16x16x32_f16 v[74:77], v[118:121], v[142:145], v[74:77]
	s_addc_u32 s31, s31, 0
	s_add_i32 m0, s2, 0x8000
	v_mfma_f32_16x16x32_f16 v[66:69], v[110:113], v[150:153], v[66:69]
	v_mfma_f32_16x16x32_f16 v[58:61], v[118:121], v[150:153], v[58:61]
	global_load_lds_dwordx4 v84, s[30:31]
	v_mfma_f32_16x16x32_f16 v[54:57], v[106:109], v[154:157], v[54:57]
	v_mfma_f32_16x16x32_f16 v[46:49], v[114:117], v[154:157], v[46:49]
	v_mfma_f32_16x16x32_f16 v[38:41], v[106:109], v[162:165], v[38:41]
	v_mfma_f32_16x16x32_f16 v[30:33], v[114:117], v[162:165], v[30:33]
	v_mfma_f32_16x16x32_f16 v[54:57], v[110:113], v[158:161], v[54:57]
	v_mfma_f32_16x16x32_f16 v[46:49], v[118:121], v[158:161], v[46:49]
	s_add_i32 m0, s2, 0xa000
	v_mfma_f32_16x16x32_f16 v[38:41], v[110:113], v[166:169], v[38:41]
	v_mfma_f32_16x16x32_f16 v[30:33], v[118:121], v[166:169], v[30:33]
	global_load_lds_dwordx4 v88, s[30:31]
	v_mfma_f32_16x16x32_f16 v[70:73], v[122:125], v[138:141], v[70:73]
	v_mfma_f32_16x16x32_f16 v[62:65], v[130:133], v[138:141], v[62:65]
	v_mfma_f32_16x16x32_f16 v[50:53], v[122:125], v[146:149], v[50:53]
	v_mfma_f32_16x16x32_f16 v[42:45], v[130:133], v[146:149], v[42:45]
	v_mfma_f32_16x16x32_f16 v[70:73], v[126:129], v[142:145], v[70:73]
	v_mfma_f32_16x16x32_f16 v[62:65], v[134:137], v[142:145], v[62:65]
	s_add_i32 m0, s2, 0x2000
	v_mfma_f32_16x16x32_f16 v[50:53], v[126:129], v[150:153], v[50:53]
	v_mfma_f32_16x16x32_f16 v[42:45], v[134:137], v[150:153], v[42:45]
	global_load_lds_dwordx4 v86, s[34:35]
	v_mfma_f32_16x16x32_f16 v[34:37], v[122:125], v[154:157], v[34:37]
	v_mfma_f32_16x16x32_f16 v[26:29], v[130:133], v[154:157], v[26:29]
	v_mfma_f32_16x16x32_f16 v[18:21], v[122:125], v[162:165], v[18:21]
	v_mfma_f32_16x16x32_f16 v[10:13], v[130:133], v[162:165], v[10:13]
	v_mfma_f32_16x16x32_f16 v[34:37], v[126:129], v[158:161], v[34:37]
	v_mfma_f32_16x16x32_f16 v[26:29], v[134:137], v[158:161], v[26:29]
	v_mfma_f32_16x16x32_f16 v[18:21], v[126:129], v[166:169], v[18:21]
	v_mfma_f32_16x16x32_f16 v[10:13], v[134:137], v[166:169], v[10:13]
	s_setprio 0
	s_add_i32 s2, s14, 1
	s_cmp_lt_u32 s25, 2
	s_cselect_b64 s[30:31], -1, 0
	s_cmp_eq_u32 s2, 16
	s_cselect_b64 s[34:35], -1, 0
	s_and_b64 s[36:37], s[34:35], exec
	s_cselect_b32 s14, 0, s2
	s_and_b64 s[30:31], s[34:35], s[30:31]
	s_cmp_lg_u64 s[30:31], 0
	s_addc_u32 s25, s25, 0
	s_barrier
	s_add_i32 s26, s26, -1
	s_mov_b32 s2, s15
	s_mov_b32 s15, s27
	s_cmp_lg_u32 s26, 0
	s_mov_b32 s27, s28
	s_cbranch_scc1 .LBB1_5
	s_ashr_i32 s2, s17, 7
	s_and_b32 s3, s2, -16
	s_or_b32 s2, s3, 2
	s_sub_u32 s14, s10, s8
	s_subb_u32 s11, s11, s9
	s_bfe_u32 s6, s17, 0x50006
	s_add_u32 s14, s8, s14
	s_addc_u32 s15, s9, s11
	s_lshr_b32 s11, s24, 6
	s_or_b32 s17, s11, s3
	s_lshl_b32 s17, s17, 8
	s_lshl_b32 s23, s6, 3
	v_bfe_u32 v93, v105, 3, 3
	v_pk_add_f32 v[80:81], v[24:25], v[80:81]
	v_pk_add_f32 v[78:79], v[22:23], v[78:79]
	v_pk_add_f32 v[74:75], v[14:15], v[74:75]
	s_or_b32 s17, s17, s23
	s_or_b32 s11, s2, s11
	v_cvt_pk_f16_f32 v78, v78, v79
	v_cvt_pk_f16_f32 v79, v80, v81
	v_cvt_pk_f16_f32 v80, v74, v75
	v_or_b32_e32 v74, s17, v93
	s_lshl_b32 s11, s11, 8
	v_ashrrev_i32_e32 v75, 31, v74
	v_pk_add_f32 v[72:73], v[8:9], v[72:73]
	v_pk_add_f32 v[70:71], v[6:7], v[70:71]
	v_pk_add_f32 v[62:63], v[2:3], v[62:63]
	s_or_b32 s11, s11, s23
	v_lshlrev_b64 v[74:75], 10, v[74:75]
	v_cvt_pk_f16_f32 v70, v70, v71
	v_cvt_pk_f16_f32 v71, v72, v73
	v_cvt_pk_f16_f32 v72, v62, v63
	v_or_b32_e32 v62, s11, v93
	v_pk_add_f32 v[76:77], v[16:17], v[76:77]
	v_lshl_add_u64 v[74:75], s[14:15], 0, v[74:75]
	v_ashrrev_i32_e32 v63, 31, v62
	v_cvt_pk_f16_f32 v81, v76, v77
	v_lshl_add_u64 v[76:77], v[74:75], 0, v[98:99]
	v_lshlrev_b64 v[62:63], 10, v[62:63]
	global_store_dwordx4 v[76:77], v[78:81], off sc1
	v_pk_add_f32 v[64:65], v[4:5], v[64:65]
	v_lshl_add_u64 v[76:77], s[14:15], 0, v[62:63]
	v_cvt_pk_f16_f32 v73, v64, v65
	v_lshl_add_u64 v[62:63], v[76:77], 0, v[98:99]
	global_store_dwordx4 v[62:63], v[70:73], off sc1
	v_pk_add_f32 v[64:65], v[24:25], v[68:69]
	v_pk_add_f32 v[62:63], v[22:23], v[66:67]
	v_pk_add_f32 v[60:61], v[16:17], v[60:61]
	v_pk_add_f32 v[58:59], v[14:15], v[58:59]
	v_pk_add_f32 v[52:53], v[8:9], v[52:53]
	v_pk_add_f32 v[50:51], v[6:7], v[50:51]
	v_pk_add_f32 v[44:45], v[4:5], v[44:45]
	v_pk_add_f32 v[42:43], v[2:3], v[42:43]
	v_cvt_pk_f16_f32 v62, v62, v63
	v_cvt_pk_f16_f32 v63, v64, v65
	v_cvt_pk_f16_f32 v64, v58, v59
	v_cvt_pk_f16_f32 v65, v60, v61
	v_lshl_add_u64 v[58:59], v[74:75], 0, v[96:97]
	v_cvt_pk_f16_f32 v50, v50, v51
	v_cvt_pk_f16_f32 v51, v52, v53
	v_cvt_pk_f16_f32 v52, v42, v43
	v_cvt_pk_f16_f32 v53, v44, v45
	v_lshl_add_u64 v[42:43], v[76:77], 0, v[96:97]
	v_mov_b32_e32 v1, 0
	global_store_dwordx4 v[58:59], v[62:65], off sc1
	global_store_dwordx4 v[42:43], v[50:53], off sc1
	v_pk_add_f32 v[44:45], v[24:25], v[56:57]
	v_pk_add_f32 v[42:43], v[22:23], v[54:55]
	v_mov_b32_e32 v95, v1
	v_cvt_pk_f16_f32 v42, v42, v43
	v_cvt_pk_f16_f32 v43, v44, v45
	v_pk_add_f32 v[48:49], v[16:17], v[48:49]
	v_pk_add_f32 v[44:45], v[14:15], v[46:47]
	v_pk_add_f32 v[36:37], v[8:9], v[36:37]
	v_pk_add_f32 v[34:35], v[6:7], v[34:35]
	v_pk_add_f32 v[28:29], v[4:5], v[28:29]
	v_pk_add_f32 v[26:27], v[2:3], v[26:27]
	v_pk_add_f32 v[24:25], v[24:25], v[40:41]
	v_pk_add_f32 v[22:23], v[22:23], v[38:39]
	v_pk_add_f32 v[16:17], v[16:17], v[32:33]
	v_pk_add_f32 v[14:15], v[14:15], v[30:31]
	v_pk_add_f32 v[8:9], v[8:9], v[20:21]
	v_pk_add_f32 v[6:7], v[6:7], v[18:19]
	v_pk_add_f32 v[4:5], v[4:5], v[12:13]
	v_pk_add_f32 v[2:3], v[2:3], v[10:11]
	s_add_u32 s14, s20, s22
	v_cvt_pk_f16_f32 v44, v44, v45
	v_cvt_pk_f16_f32 v45, v48, v49
	v_lshl_add_u64 v[46:47], v[74:75], 0, v[0:1]
	v_cvt_pk_f16_f32 v34, v34, v35
	v_cvt_pk_f16_f32 v35, v36, v37
	v_cvt_pk_f16_f32 v36, v26, v27
	v_cvt_pk_f16_f32 v37, v28, v29
	v_lshl_add_u64 v[26:27], v[76:77], 0, v[0:1]
	v_cvt_pk_f16_f32 v22, v22, v23
	v_cvt_pk_f16_f32 v23, v24, v25
	v_cvt_pk_f16_f32 v24, v14, v15
	v_cvt_pk_f16_f32 v25, v16, v17
	v_lshl_add_u64 v[14:15], v[74:75], 0, v[94:95]
	v_cvt_pk_f16_f32 v6, v6, v7
	v_cvt_pk_f16_f32 v7, v8, v9
	v_cvt_pk_f16_f32 v8, v2, v3
	v_cvt_pk_f16_f32 v9, v4, v5
	v_lshl_add_u64 v[2:3], v[76:77], 0, v[94:95]
	s_addc_u32 s15, s21, 0
	v_mov_b32_e32 v93, v1
	global_store_dwordx4 v[46:47], v[42:45], off sc1
	global_store_dwordx4 v[26:27], v[34:37], off sc1
	global_store_dwordx4 v[14:15], v[22:25], off sc1
	global_store_dwordx4 v[2:3], v[6:9], off sc1
	v_lshl_add_u64 v[2:3], s[14:15], 0, v[92:93]
	s_mov_b64 s[14:15], 0x2000
	v_lshl_add_u64 v[2:3], v[2:3], 0, s[14:15]
	global_load_dwordx4 v[20:23], v[2:3], off
	global_load_dwordx4 v[12:15], v[2:3], off offset:16
	global_load_dwordx4 v[8:11], v[2:3], off offset:512
	global_load_dwordx4 v[4:7], v[2:3], off offset:528
	s_add_u32 s11, s12, 0x400000
	s_mov_b32 s7, 2
	v_and_b32_e32 v106, 56, v105
	s_mov_b32 s10, 0
	s_addc_u32 s12, s13, 0
	s_mov_b32 s14, 0xc000
	s_mov_b32 s17, 0x18000
	s_mov_b32 s13, 16
	v_mov_b32_e32 v0, v1
	v_mov_b32_e32 v2, v1
	v_mov_b32_e32 v3, v1
	v_mov_b32_e32 v16, v1
	v_mov_b32_e32 v17, v1
	v_mov_b32_e32 v18, v1
	v_mov_b32_e32 v19, v1
	v_mov_b32_e32 v24, v1
	v_mov_b32_e32 v25, v1
	v_mov_b32_e32 v26, v1
	v_mov_b32_e32 v27, v1
	v_mov_b32_e32 v32, v1
	v_mov_b32_e32 v33, v1
	v_mov_b32_e32 v34, v1
	v_mov_b32_e32 v35, v1
	v_mov_b32_e32 v40, v1
	v_mov_b32_e32 v41, v1
	v_mov_b32_e32 v42, v1
	v_mov_b32_e32 v43, v1
	v_mov_b32_e32 v48, v1
	v_mov_b32_e32 v49, v1
	v_mov_b32_e32 v50, v1
	v_mov_b32_e32 v51, v1
	v_mov_b32_e32 v60, v1
	v_mov_b32_e32 v61, v1
	v_mov_b32_e32 v62, v1
	v_mov_b32_e32 v63, v1
	v_mov_b32_e32 v68, v1
	v_mov_b32_e32 v69, v1
	v_mov_b32_e32 v70, v1
	v_mov_b32_e32 v71, v1
	v_mov_b32_e32 v28, v1
	v_mov_b32_e32 v29, v1
	v_mov_b32_e32 v30, v1
	v_mov_b32_e32 v31, v1
	v_mov_b32_e32 v36, v1
	v_mov_b32_e32 v37, v1
	v_mov_b32_e32 v38, v1
	v_mov_b32_e32 v39, v1
	v_mov_b32_e32 v44, v1
	v_mov_b32_e32 v45, v1
	v_mov_b32_e32 v46, v1
	v_mov_b32_e32 v47, v1
	v_mov_b32_e32 v52, v1
	v_mov_b32_e32 v53, v1
	v_mov_b32_e32 v54, v1
	v_mov_b32_e32 v55, v1
	v_mov_b32_e32 v56, v1
	v_mov_b32_e32 v57, v1
	v_mov_b32_e32 v58, v1
	v_mov_b32_e32 v59, v1
	v_mov_b32_e32 v64, v1
	v_mov_b32_e32 v65, v1
	v_mov_b32_e32 v66, v1
	v_mov_b32_e32 v67, v1
	v_mov_b32_e32 v72, v1
	v_mov_b32_e32 v73, v1
	v_mov_b32_e32 v74, v1
	v_mov_b32_e32 v75, v1
	v_mov_b32_e32 v76, v1
	v_mov_b32_e32 v77, v1
	v_mov_b32_e32 v78, v1
	v_mov_b32_e32 v79, v1
.LBB1_7:
	s_mov_b32 s15, s17
	v_add_u32_e32 v80, s15, v101
	ds_read_b128 v[92:95], v80 offset:16384
	ds_read_b128 v[96:99], v80 offset:17408
	ds_read_b128 v[108:111], v80 offset:18432
	ds_read_b128 v[112:115], v80 offset:19456
	ds_read_b128 v[116:119], v80 offset:32768
	ds_read_b128 v[120:123], v80 offset:33792
	ds_read_b128 v[124:127], v80 offset:34816
	ds_read_b128 v[128:131], v80 offset:35840
	v_add_u32_e32 v80, s15, v91
	ds_read_b128 v[132:135], v80
	ds_read_b128 v[136:139], v80 offset:1024
	ds_read_b128 v[140:143], v80 offset:2048
	ds_read_b128 v[144:147], v80 offset:3072
	ds_read_b128 v[148:151], v80 offset:4096
	ds_read_b128 v[152:155], v80 offset:5120
	ds_read_b128 v[156:159], v80 offset:6144
	ds_read_b128 v[160:163], v80 offset:7168
	s_lshl_b32 s17, s7, 7
	s_ashr_i32 s23, s17, 31
	s_add_u32 s20, s11, s17
	s_addc_u32 s21, s12, s23
	s_add_u32 s22, s4, s17
	s_addc_u32 s23, s5, s23
	s_add_i32 s17, s19, s14
	s_add_i32 m0, s17, 0x4000
	s_nop 0
	global_load_lds_dwordx4 v84, s[20:21]
	s_add_i32 m0, s17, 0x6000
	s_nop 0
	global_load_lds_dwordx4 v88, s[20:21]
	s_mov_b32 m0, s17
	s_nop 0
	global_load_lds_dwordx4 v82, s[22:23]
	s_waitcnt vmcnt(3)
	s_waitcnt lgkmcnt(0)
	s_barrier
	s_setprio 1
	s_waitcnt lgkmcnt(0)
	v_mfma_f32_16x16x32_f16 v[76:79], v[92:95], v[132:135], v[76:79]
	v_mfma_f32_16x16x32_f16 v[72:75], v[108:111], v[132:135], v[72:75]
	v_mfma_f32_16x16x32_f16 v[64:67], v[92:95], v[140:143], v[64:67]
	v_mfma_f32_16x16x32_f16 v[56:59], v[108:111], v[140:143], v[56:59]
	v_mfma_f32_16x16x32_f16 v[76:79], v[96:99], v[136:139], v[76:79]
	s_add_u32 s20, s20, 0x40000
	v_mfma_f32_16x16x32_f16 v[72:75], v[112:115], v[136:139], v[72:75]
	s_addc_u32 s21, s21, 0
	s_add_i32 m0, s17, 0x8000
	v_mfma_f32_16x16x32_f16 v[64:67], v[96:99], v[144:147], v[64:67]
	v_mfma_f32_16x16x32_f16 v[56:59], v[112:115], v[144:147], v[56:59]
	global_load_lds_dwordx4 v84, s[20:21]
	v_mfma_f32_16x16x32_f16 v[52:55], v[92:95], v[148:151], v[52:55]
	v_mfma_f32_16x16x32_f16 v[44:47], v[108:111], v[148:151], v[44:47]
	v_mfma_f32_16x16x32_f16 v[36:39], v[92:95], v[156:159], v[36:39]
	v_mfma_f32_16x16x32_f16 v[28:31], v[108:111], v[156:159], v[28:31]
	v_mfma_f32_16x16x32_f16 v[52:55], v[96:99], v[152:155], v[52:55]
	v_mfma_f32_16x16x32_f16 v[44:47], v[112:115], v[152:155], v[44:47]
	s_add_i32 m0, s17, 0xa000
	v_mfma_f32_16x16x32_f16 v[36:39], v[96:99], v[160:163], v[36:39]
	v_mfma_f32_16x16x32_f16 v[28:31], v[112:115], v[160:163], v[28:31]
	global_load_lds_dwordx4 v88, s[20:21]
	v_mfma_f32_16x16x32_f16 v[68:71], v[116:119], v[132:135], v[68:71]
	v_mfma_f32_16x16x32_f16 v[60:63], v[124:127], v[132:135], v[60:63]
	v_mfma_f32_16x16x32_f16 v[48:51], v[116:119], v[140:143], v[48:51]
	v_mfma_f32_16x16x32_f16 v[40:43], v[124:127], v[140:143], v[40:43]
	v_mfma_f32_16x16x32_f16 v[68:71], v[120:123], v[136:139], v[68:71]
	v_mfma_f32_16x16x32_f16 v[60:63], v[128:131], v[136:139], v[60:63]
	s_add_i32 m0, s17, 0x2000
	v_mfma_f32_16x16x32_f16 v[48:51], v[120:123], v[144:147], v[48:51]
	v_mfma_f32_16x16x32_f16 v[40:43], v[128:131], v[144:147], v[40:43]
	global_load_lds_dwordx4 v86, s[22:23]
	v_mfma_f32_16x16x32_f16 v[32:35], v[116:119], v[148:151], v[32:35]
	v_mfma_f32_16x16x32_f16 v[24:27], v[124:127], v[148:151], v[24:27]
	v_mfma_f32_16x16x32_f16 v[16:19], v[116:119], v[156:159], v[16:19]
	v_mfma_f32_16x16x32_f16 v[0:3], v[124:127], v[156:159], v[0:3]
	v_mfma_f32_16x16x32_f16 v[32:35], v[120:123], v[152:155], v[32:35]
	v_mfma_f32_16x16x32_f16 v[24:27], v[128:131], v[152:155], v[24:27]
	v_mfma_f32_16x16x32_f16 v[16:19], v[120:123], v[160:163], v[16:19]
	v_mfma_f32_16x16x32_f16 v[0:3], v[128:131], v[160:163], v[0:3]
	s_setprio 0
	s_add_i32 s7, s7, 1
	s_cmp_lg_u32 s7, 16
	s_cselect_b32 s7, s7, 0
	s_barrier
	s_add_i32 s13, s13, -1
	s_mov_b32 s17, s10
	s_mov_b32 s10, s14
	s_cmp_lg_u32 s13, 0
	s_mov_b32 s14, s15
	s_cbranch_scc1 .LBB1_7
	s_sub_u32 s0, s0, s8
	s_subb_u32 s1, s1, s9
	s_add_u32 s0, s8, s0
	s_addc_u32 s1, s9, s1
	s_lshl_b32 s3, s3, 6
	s_or_b32 s3, s3, s16
	s_lshl_b32 s4, s6, 1
	v_lshrrev_b32_e32 v86, 5, v106
	v_pk_add_f32 v[78:79], v[22:23], v[78:79]
	v_pk_add_f32 v[76:77], v[20:21], v[76:77]
	v_pk_add_f32 v[72:73], v[12:13], v[72:73]
	s_or_b32 s3, s3, s4
	s_lshl_b32 s2, s2, 6
	v_cvt_pk_f16_f32 v76, v76, v77
	v_cvt_pk_f16_f32 v77, v78, v79
	v_cvt_pk_f16_f32 v78, v72, v73
	v_or_b32_e32 v72, s3, v86
	s_or_b32 s2, s2, s16
	v_ashrrev_i32_e32 v73, 31, v72
	v_pk_add_f32 v[70:71], v[10:11], v[70:71]
	v_pk_add_f32 v[68:69], v[8:9], v[68:69]
	v_pk_add_f32 v[60:61], v[4:5], v[60:61]
	s_or_b32 s2, s2, s4
	v_lshlrev_b64 v[72:73], 12, v[72:73]
	v_cvt_pk_f16_f32 v68, v68, v69
	v_cvt_pk_f16_f32 v69, v70, v71
	v_cvt_pk_f16_f32 v70, v60, v61
	v_or_b32_e32 v60, s2, v86
	v_mov_b32_e32 v91, 0
	v_pk_add_f32 v[74:75], v[14:15], v[74:75]
	v_lshl_add_u64 v[72:73], s[0:1], 0, v[72:73]
	v_ashrrev_i32_e32 v61, 31, v60
	v_cvt_pk_f16_f32 v79, v74, v75
	v_lshl_add_u64 v[74:75], v[72:73], 0, v[90:91]
	v_lshlrev_b64 v[60:61], 12, v[60:61]
	v_lshl_or_b32 v84, v102, 6, v100
	v_mov_b32_e32 v85, v91
	global_store_dwordx4 v[74:75], v[76:79], off sc1
	v_lshl_add_u64 v[74:75], s[0:1], 0, v[60:61]
	v_pk_add_f32 v[50:51], v[10:11], v[50:51]
	v_pk_add_f32 v[48:49], v[8:9], v[48:49]
	v_pk_add_f32 v[42:43], v[6:7], v[42:43]
	v_pk_add_f32 v[40:41], v[4:5], v[40:41]
	v_pk_add_f32 v[62:63], v[6:7], v[62:63]
	v_cvt_pk_f16_f32 v48, v48, v49
	v_cvt_pk_f16_f32 v49, v50, v51
	v_cvt_pk_f16_f32 v50, v40, v41
	v_cvt_pk_f16_f32 v51, v42, v43
	v_lshl_add_u64 v[40:41], v[74:75], 0, v[84:85]
	v_cvt_pk_f16_f32 v71, v62, v63
	v_lshl_add_u64 v[60:61], v[74:75], 0, v[90:91]
	global_store_dwordx4 v[40:41], v[48:51], off sc1
	v_pk_add_f32 v[42:43], v[22:23], v[54:55]
	v_pk_add_f32 v[40:41], v[20:21], v[52:53]
	v_lshl_or_b32 v80, v103, 6, v100
	v_lshl_or_b32 v82, v104, 6, v100
	v_mov_b32_e32 v81, v91
	v_mov_b32_e32 v83, v91
	global_store_dwordx4 v[60:61], v[68:71], off sc1
	v_pk_add_f32 v[62:63], v[22:23], v[66:67]
	v_pk_add_f32 v[60:61], v[20:21], v[64:65]
	v_pk_add_f32 v[58:59], v[14:15], v[58:59]
	v_pk_add_f32 v[56:57], v[12:13], v[56:57]
	v_cvt_pk_f16_f32 v40, v40, v41
	v_cvt_pk_f16_f32 v41, v42, v43
	v_pk_add_f32 v[46:47], v[14:15], v[46:47]
	v_pk_add_f32 v[42:43], v[12:13], v[44:45]
	v_pk_add_f32 v[34:35], v[10:11], v[34:35]
	v_pk_add_f32 v[32:33], v[8:9], v[32:33]
	v_pk_add_f32 v[26:27], v[6:7], v[26:27]
	v_pk_add_f32 v[24:25], v[4:5], v[24:25]
	v_pk_add_f32 v[22:23], v[22:23], v[38:39]
	v_pk_add_f32 v[20:21], v[20:21], v[36:37]
	v_pk_add_f32 v[14:15], v[14:15], v[30:31]
	v_pk_add_f32 v[12:13], v[12:13], v[28:29]
	v_pk_add_f32 v[10:11], v[10:11], v[18:19]
	v_pk_add_f32 v[8:9], v[8:9], v[16:17]
	v_pk_add_f32 v[2:3], v[6:7], v[2:3]
	v_pk_add_f32 v[0:1], v[4:5], v[0:1]
	v_cvt_pk_f16_f32 v60, v60, v61
	v_cvt_pk_f16_f32 v61, v62, v63
	v_cvt_pk_f16_f32 v62, v56, v57
	v_cvt_pk_f16_f32 v63, v58, v59
	v_lshl_add_u64 v[56:57], v[72:73], 0, v[84:85]
	v_cvt_pk_f16_f32 v42, v42, v43
	v_cvt_pk_f16_f32 v43, v46, v47
	v_lshl_add_u64 v[44:45], v[72:73], 0, v[80:81]
	v_cvt_pk_f16_f32 v32, v32, v33
	v_cvt_pk_f16_f32 v33, v34, v35
	v_cvt_pk_f16_f32 v34, v24, v25
	v_cvt_pk_f16_f32 v35, v26, v27
	v_lshl_add_u64 v[24:25], v[74:75], 0, v[80:81]
	v_cvt_pk_f16_f32 v20, v20, v21
	v_cvt_pk_f16_f32 v21, v22, v23
	v_cvt_pk_f16_f32 v22, v12, v13
	v_cvt_pk_f16_f32 v23, v14, v15
	v_lshl_add_u64 v[12:13], v[72:73], 0, v[82:83]
	v_cvt_pk_f16_f32 v8, v8, v9
	v_cvt_pk_f16_f32 v9, v10, v11
	v_cvt_pk_f16_f32 v10, v0, v1
	v_cvt_pk_f16_f32 v11, v2, v3
	v_lshl_add_u64 v[0:1], v[74:75], 0, v[82:83]
	global_store_dwordx4 v[56:57], v[60:63], off sc1
	global_store_dwordx4 v[44:45], v[40:43], off sc1
	global_store_dwordx4 v[24:25], v[32:35], off sc1
	global_store_dwordx4 v[12:13], v[20:23], off sc1
	global_store_dwordx4 v[0:1], v[8:11], off sc1
	s_waitcnt vmcnt(0)
	s_cmpk_gt_u32 s18, 0xff
	s_cbranch_scc1 .LBB1_10
	s_barrier

.LBB2_3:
	s_mov_b32 s16, s15
	v_add_u32_e32 v116, s16, v87
	v_add_u32_e32 v148, s16, v0
	ds_read_b128 v[88:91], v116 offset:16384
	ds_read_b128 v[92:95], v116 offset:17408
	ds_read_b128 v[96:99], v116 offset:18432
	ds_read_b128 v[100:103], v116 offset:19456
	ds_read_b128 v[104:107], v116 offset:32768
	ds_read_b128 v[108:111], v116 offset:33792
	ds_read_b128 v[112:115], v116 offset:34816
	ds_read_b128 v[116:119], v116 offset:35840
	ds_read_b128 v[120:123], v148
	ds_read_b128 v[124:127], v148 offset:1024
	ds_read_b128 v[128:131], v148 offset:2048
	ds_read_b128 v[132:135], v148 offset:3072
	ds_read_b128 v[136:139], v148 offset:4096
	ds_read_b128 v[140:143], v148 offset:5120
	ds_read_b128 v[144:147], v148 offset:6144
	ds_read_b128 v[148:151], v148 offset:7168
	s_lshl_b32 s15, s7, 7
	s_ashr_i32 s17, s15, 31
	s_add_u32 s18, s4, s15
	s_addc_u32 s19, s5, s17
	s_add_u32 s20, s2, s15
	s_addc_u32 s21, s3, s17
	s_add_i32 s15, s6, s14
	s_add_i32 m0, s15, 0x4000
	s_nop 0
	global_load_lds_dwordx4 v82, s[18:19]
	s_add_i32 m0, s15, 0x6000
	s_nop 0
	global_load_lds_dwordx4 v84, s[18:19]
	s_mov_b32 m0, s15
	s_nop 0
	global_load_lds_dwordx4 v82, s[20:21]
	s_waitcnt vmcnt(3)
	s_waitcnt lgkmcnt(0)
	s_barrier
	s_setprio 1
	s_waitcnt lgkmcnt(0)
	v_mfma_f32_16x16x32_f16 v[18:21], v[88:91], v[120:123], v[18:21]
	v_mfma_f32_16x16x32_f16 v[70:73], v[96:99], v[120:123], v[70:73]
	v_mfma_f32_16x16x32_f16 v[58:61], v[88:91], v[128:131], v[58:61]
	v_mfma_f32_16x16x32_f16 v[54:57], v[96:99], v[128:131], v[54:57]
	v_mfma_f32_16x16x32_f16 v[18:21], v[92:95], v[124:127], v[18:21]
	s_add_u32 s18, s18, 0x40000
	v_mfma_f32_16x16x32_f16 v[70:73], v[100:103], v[124:127], v[70:73]
	s_addc_u32 s19, s19, 0
	s_add_i32 m0, s15, 0x8000
	v_mfma_f32_16x16x32_f16 v[58:61], v[92:95], v[132:135], v[58:61]
	v_mfma_f32_16x16x32_f16 v[54:57], v[100:103], v[132:135], v[54:57]
	global_load_lds_dwordx4 v82, s[18:19]
	v_mfma_f32_16x16x32_f16 v[42:45], v[88:91], v[136:139], v[42:45]
	v_mfma_f32_16x16x32_f16 v[38:41], v[96:99], v[136:139], v[38:41]
	v_mfma_f32_16x16x32_f16 v[26:29], v[88:91], v[144:147], v[26:29]
	v_mfma_f32_16x16x32_f16 v[22:25], v[96:99], v[144:147], v[22:25]
	v_mfma_f32_16x16x32_f16 v[42:45], v[92:95], v[140:143], v[42:45]
	v_mfma_f32_16x16x32_f16 v[38:41], v[100:103], v[140:143], v[38:41]
	s_add_i32 m0, s15, 0xa000
	v_mfma_f32_16x16x32_f16 v[26:29], v[92:95], v[148:151], v[26:29]
	v_mfma_f32_16x16x32_f16 v[22:25], v[100:103], v[148:151], v[22:25]
	global_load_lds_dwordx4 v84, s[18:19]
	v_mfma_f32_16x16x32_f16 v[78:81], v[104:107], v[120:123], v[78:81]
	v_mfma_f32_16x16x32_f16 v[74:77], v[112:115], v[120:123], v[74:77]
	v_mfma_f32_16x16x32_f16 v[66:69], v[104:107], v[128:131], v[66:69]
	v_mfma_f32_16x16x32_f16 v[62:65], v[112:115], v[128:131], v[62:65]
	v_mfma_f32_16x16x32_f16 v[78:81], v[108:111], v[124:127], v[78:81]
	v_mfma_f32_16x16x32_f16 v[74:77], v[116:119], v[124:127], v[74:77]
	s_add_i32 m0, s15, 0x2000
	v_mfma_f32_16x16x32_f16 v[66:69], v[108:111], v[132:135], v[66:69]
	v_mfma_f32_16x16x32_f16 v[62:65], v[116:119], v[132:135], v[62:65]
	global_load_lds_dwordx4 v84, s[20:21]
	v_mfma_f32_16x16x32_f16 v[50:53], v[104:107], v[136:139], v[50:53]
	v_mfma_f32_16x16x32_f16 v[46:49], v[112:115], v[136:139], v[46:49]
	v_mfma_f32_16x16x32_f16 v[34:37], v[104:107], v[144:147], v[34:37]
	v_mfma_f32_16x16x32_f16 v[30:33], v[112:115], v[144:147], v[30:33]
	v_mfma_f32_16x16x32_f16 v[50:53], v[108:111], v[140:143], v[50:53]
	v_mfma_f32_16x16x32_f16 v[46:49], v[116:119], v[140:143], v[46:49]
	v_mfma_f32_16x16x32_f16 v[34:37], v[108:111], v[148:151], v[34:37]
	v_mfma_f32_16x16x32_f16 v[30:33], v[116:119], v[148:151], v[30:33]
	s_setprio 0
	s_add_i32 s7, s7, 1
	s_cmp_lg_u32 s7, 16
	s_cselect_b32 s7, s7, 0
	s_barrier
	s_add_i32 s11, s11, -1
	s_mov_b32 s15, s13
	s_mov_b32 s13, s14
	s_cmp_lg_u32 s11, 0
	s_mov_b32 s14, s16
	s_cbranch_scc1 .LBB2_3
	v_lshl_add_u32 v0, s0, 7, v86
	v_or_b32_e32 v88, s10, v1
	v_ashrrev_i32_e32 v1, 31, v0
	v_lshlrev_b64 v[82:83], 12, v[0:1]
	v_or_b32_e32 v88, s1, v88
	v_lshl_add_u64 v[82:83], s[8:9], 0, v[82:83]
	v_lshlrev_b32_e32 v88, 2, v88
	v_mov_b32_e32 v89, 0
	v_or_b32_e32 v84, 16, v0
	v_lshl_add_u64 v[82:83], v[82:83], 0, v[88:89]
	v_pk_add_f32 v[20:21], v[16:17], v[20:21]
	v_pk_add_f32 v[18:19], v[14:15], v[18:19]
	v_ashrrev_i32_e32 v85, 31, v84
	global_store_dwordx4 v[82:83], v[18:21], off sc1
	v_lshlrev_b64 v[84:85], 12, v[84:85]
	v_lshl_add_u64 v[84:85], s[8:9], 0, v[84:85]
	v_pk_add_f32 v[20:21], v[12:13], v[72:73]
	v_pk_add_f32 v[18:19], v[10:11], v[70:71]
	global_store_dwordx4 v[82:83], v[18:21], off offset:64 sc1
	v_or_b32_e32 v86, 32, v0
	v_lshl_add_u64 v[84:85], v[84:85], 0, v[88:89]
	v_pk_add_f32 v[20:21], v[8:9], v[80:81]
	v_pk_add_f32 v[18:19], v[6:7], v[78:79]
	global_store_dwordx4 v[82:83], v[18:21], off offset:512 sc1
	v_ashrrev_i32_e32 v87, 31, v86
	v_lshlrev_b64 v[86:87], 12, v[86:87]
	v_pk_add_f32 v[20:21], v[4:5], v[76:77]
	v_pk_add_f32 v[18:19], v[2:3], v[74:75]
	global_store_dwordx4 v[82:83], v[18:21], off offset:576 sc1
	v_lshl_add_u64 v[86:87], s[8:9], 0, v[86:87]
	v_or_b32_e32 v0, 48, v0
	v_pk_add_f32 v[20:21], v[16:17], v[60:61]
	v_pk_add_f32 v[18:19], v[14:15], v[58:59]
	global_store_dwordx4 v[84:85], v[18:21], off sc1
	v_ashrrev_i32_e32 v1, 31, v0
	v_lshl_add_u64 v[86:87], v[86:87], 0, v[88:89]
	v_pk_add_f32 v[20:21], v[12:13], v[56:57]
	v_pk_add_f32 v[18:19], v[10:11], v[54:55]
	global_store_dwordx4 v[84:85], v[18:21], off offset:64 sc1
	v_lshlrev_b64 v[0:1], 12, v[0:1]
	v_lshl_add_u64 v[0:1], s[8:9], 0, v[0:1]
	v_pk_add_f32 v[20:21], v[8:9], v[68:69]
	v_pk_add_f32 v[18:19], v[6:7], v[66:67]
	global_store_dwordx4 v[84:85], v[18:21], off offset:512 sc1
	v_lshl_add_u64 v[0:1], v[0:1], 0, v[88:89]
	s_cmpk_gt_u32 s12, 0xff
	v_pk_add_f32 v[20:21], v[4:5], v[64:65]
	v_pk_add_f32 v[18:19], v[2:3], v[62:63]
	global_store_dwordx4 v[84:85], v[18:21], off offset:576 sc1
	s_nop 1
	v_pk_add_f32 v[20:21], v[16:17], v[44:45]
	v_pk_add_f32 v[18:19], v[14:15], v[42:43]
	global_store_dwordx4 v[86:87], v[18:21], off sc1
	v_pk_add_f32 v[16:17], v[16:17], v[28:29]
	v_pk_add_f32 v[14:15], v[14:15], v[26:27]
	v_pk_add_f32 v[20:21], v[12:13], v[40:41]
	v_pk_add_f32 v[18:19], v[10:11], v[38:39]
	global_store_dwordx4 v[86:87], v[18:21], off offset:64 sc1
	v_pk_add_f32 v[12:13], v[12:13], v[24:25]
	v_pk_add_f32 v[10:11], v[10:11], v[22:23]
	v_pk_add_f32 v[20:21], v[8:9], v[52:53]
	v_pk_add_f32 v[18:19], v[6:7], v[50:51]
	global_store_dwordx4 v[86:87], v[18:21], off offset:512 sc1
	v_pk_add_f32 v[8:9], v[8:9], v[36:37]
	v_pk_add_f32 v[6:7], v[6:7], v[34:35]
	v_pk_add_f32 v[20:21], v[4:5], v[48:49]
	v_pk_add_f32 v[18:19], v[2:3], v[46:47]
	v_pk_add_f32 v[4:5], v[4:5], v[32:33]
	v_pk_add_f32 v[2:3], v[2:3], v[30:31]
	global_store_dwordx4 v[86:87], v[18:21], off offset:576 sc1
	global_store_dwordx4 v[0:1], v[14:17], off sc1
	global_store_dwordx4 v[0:1], v[10:13], off offset:64 sc1
	global_store_dwordx4 v[0:1], v[6:9], off offset:512 sc1
	global_store_dwordx4 v[0:1], v[2:5], off offset:576 sc1
	s_waitcnt vmcnt(0)
	s_cbranch_scc1 .LBB2_6
	s_barrier
